# workgroups that counted themselves early skip the tail queue check; mixer HGRN2 units signal 4 chunks before their end
# baseline (speedup 1.0000x reference)
.LBB0_317:
	v_readlane_b32 s100, v255, 63
	v_writelane_b32 v255, 0, 63
	s_add_u32 s4, s0, 0x5100
	s_addc_u32 s5, s1, 0
	s_waitcnt vmcnt(0) lgkmcnt(0)
	s_barrier
	s_cmp_lg_u32 s100, 0
	s_cbranch_scc1 .LBB0_375
	s_mov_b64 s[6:7], exec
	v_readlane_b32 s8, v253, 4
	v_readlane_b32 s9, v253, 5
	s_and_b64 s[8:9], s[6:7], s[8:9]
	s_mov_b64 exec, s[8:9]
	s_cbranch_execz .LBB0_320
	s_mov_b64 s[8:9], exec
	v_mbcnt_lo_u32_b32 v1, s8, 0
	v_mbcnt_hi_u32_b32 v1, s9, v1
	v_cmp_eq_u32_e32 vcc, 0, v1
	s_and_b64 s[16:17], exec, vcc
	s_mov_b64 exec, s[16:17]
	s_cbranch_execz .LBB0_320
	s_bcnt1_i32_b64 s2, s[8:9]
	v_mov_b32_e32 v1, s2
	global_atomic_add v195, v1, s[4:5]

.LBB0_465:
	s_waitcnt lgkmcnt(0)
	s_barrier
	ds_read_b128 v[10:13], v127
	ds_read_b128 v[14:17], v127 offset:64
	ds_read_b128 v[56:59], v127 offset:128
	ds_read_b128 v[60:63], v127 offset:192
	ds_read_b128 v[64:67], v128 offset:17408
	ds_read_b128 v[68:71], v128 offset:17472
	ds_read_b128 v[72:75], v128 offset:17536
	ds_read_b128 v[76:79], v128 offset:17600
	ds_read_b128 v[176:179], v128 offset:21760
	ds_read_b128 v[180:183], v128 offset:21824
	ds_read_b128 v[184:187], v128 offset:21888
	ds_read_b128 v[188:191], v128 offset:21952
	s_waitcnt lgkmcnt(7)
	v_mfma_f32_16x16x32_bf16 v[2:5], v[64:67], v[10:13], 0
	s_waitcnt lgkmcnt(6)
	v_mfma_f32_16x16x32_bf16 v[2:5], v[68:71], v[14:17], v[2:5]
	s_waitcnt lgkmcnt(3)
	v_mfma_f32_16x16x32_bf16 v[6:9], v[176:179], v[10:13], 0
	v_mfma_f32_16x16x32_bf16 v[2:5], v[72:75], v[56:59], v[2:5]
	s_waitcnt lgkmcnt(2)
	v_mfma_f32_16x16x32_bf16 v[6:9], v[180:183], v[14:17], v[6:9]
	v_mfma_f32_16x16x32_bf16 v[2:5], v[76:79], v[60:63], v[2:5]
	s_waitcnt lgkmcnt(1)
	v_mfma_f32_16x16x32_bf16 v[6:9], v[184:187], v[56:59], v[6:9]
	s_waitcnt lgkmcnt(0)
	v_mfma_f32_16x16x32_bf16 v[6:9], v[188:191], v[60:63], v[6:9]
	s_nop 6
	v_cndmask_b32_e64 v56, v2, 0, s[44:45]
	v_cndmask_b32_e64 v57, 0, v3, s[46:47]
	v_cndmask_b32_e64 v58, v4, 0, s[48:49]
	v_cndmask_b32_e64 v59, v5, 0, s[50:51]
	v_cvt_pk_bf16_f32 v56, v56, v57
	v_cvt_pk_bf16_f32 v57, v58, v59
	ds_write_b64 v129, v[56:57]
	v_cndmask_b32_e64 v6, v6, 0, s[52:53]
	v_cndmask_b32_e64 v7, 0, v7, s[54:55]
	v_cndmask_b32_e64 v8, v8, 0, s[56:57]
	v_cndmask_b32_e64 v9, v9, 0, s[58:59]
	v_cvt_pk_bf16_f32 v6, v6, v7
	v_cvt_pk_bf16_f32 v7, v8, v9
	ds_write_b64 v130, v[6:7]
	s_waitcnt lgkmcnt(0)
	s_barrier
	ds_read_b128 v[10:13], v131
	ds_read_b128 v[14:17], v132
	ds_read_b128 v[56:59], v133
	ds_read_b128 v[60:63], v131 offset:64
	ds_read_b128 v[64:67], v132 offset:64
	ds_read_b128 v[68:71], v133 offset:64
	ds_read_b128 v[72:75], v138
	ds_read_b128 v[76:79], v134 offset:52224
	ds_read_b128 v[176:179], v137
	ds_read_b128 v[180:183], v137 offset:2304
	ds_read_b128 v[184:187], v137 offset:4608
	ds_read_b128 v[188:191], v137 offset:6912
	ds_read_b128 v[200:203], v134 offset:52288
	ds_read_b128 v[204:207], v137 offset:64
	ds_read_b128 v[208:211], v137 offset:2368
	s_waitcnt lgkmcnt(13)
	v_mfma_f32_16x16x32_bf16 v[6:9], v[10:13], v[14:17], 0
	s_waitcnt lgkmcnt(12)
	v_mfma_f32_16x16x32_bf16 v[2:5], v[10:13], v[56:59], 0
	ds_read_b128 v[212:215], v137 offset:4672
	ds_read_b128 v[220:223], v137 offset:6976
	ds_read_b128 v[224:227], v135
	s_waitcnt lgkmcnt(13)
	v_mfma_f32_16x16x32_bf16 v[6:9], v[60:63], v[64:67], v[6:9]
	s_waitcnt lgkmcnt(12)
	v_mfma_f32_16x16x32_bf16 v[2:5], v[60:63], v[68:71], v[2:5]
	ds_read_b128 v[232:235], v128
	ds_read_b128 v[236:239], v136
	ds_read_b128 v[14:17], v135 offset:64
	s_waitcnt lgkmcnt(14)
	v_pk_mul_f32 v[22:23], v[22:23], v[72:73]
	v_pk_mul_f32 v[24:25], v[24:25], v[74:75]
	v_pk_mul_f32 v[26:27], v[26:27], v[72:73]
	v_pk_mul_f32 v[28:29], v[28:29], v[74:75]
	v_pk_mul_f32 v[30:31], v[30:31], v[72:73]
	v_pk_mul_f32 v[32:33], v[32:33], v[74:75]
	v_pk_mul_f32 v[34:35], v[34:35], v[72:73]
	v_pk_mul_f32 v[36:37], v[36:37], v[74:75]
	s_waitcnt lgkmcnt(12)
	v_mfma_f32_16x16x32_bf16 v[22:25], v[76:79], v[176:179], v[22:25]
	s_waitcnt lgkmcnt(11)
	v_mfma_f32_16x16x32_bf16 v[26:29], v[76:79], v[180:183], v[26:29]
	s_waitcnt lgkmcnt(10)
	v_mfma_f32_16x16x32_bf16 v[30:33], v[76:79], v[184:187], v[30:33]
	s_waitcnt lgkmcnt(9)
	v_mfma_f32_16x16x32_bf16 v[34:37], v[76:79], v[188:191], v[34:37]
	ds_read_b128 v[10:13], v128 offset:64
	ds_read_b128 v[56:59], v136 offset:64
	ds_read_b128 v[64:67], v135 offset:128
	ds_read_b128 v[60:63], v128 offset:128
	s_waitcnt lgkmcnt(11)
	v_mfma_f32_16x16x32_bf16 v[22:25], v[200:203], v[204:207], v[22:25]
	s_waitcnt lgkmcnt(10)
	v_mfma_f32_16x16x32_bf16 v[26:29], v[200:203], v[208:211], v[26:29]
	ds_read_b128 v[68:71], v136 offset:128
	ds_read_b128 v[72:75], v135 offset:192
	s_waitcnt lgkmcnt(11)
	v_mfma_f32_16x16x32_bf16 v[30:33], v[200:203], v[212:215], v[30:33]
	s_waitcnt lgkmcnt(10)
	v_mfma_f32_16x16x32_bf16 v[34:37], v[200:203], v[220:223], v[34:37]
	ds_read_b128 v[176:179], v128 offset:192
	ds_read_b128 v[180:183], v136 offset:192
	s_waitcnt lgkmcnt(10)
	v_mfma_f32_16x16x32_bf16 v[6:9], v[224:227], v[232:235], v[6:9]
	s_waitcnt lgkmcnt(9)
	v_mfma_f32_16x16x32_bf16 v[2:5], v[224:227], v[236:239], v[2:5]
	s_waitcnt lgkmcnt(7)
	v_mfma_f32_16x16x32_bf16 v[6:9], v[14:17], v[10:13], v[6:9]
	s_waitcnt lgkmcnt(6)
	v_mfma_f32_16x16x32_bf16 v[2:5], v[14:17], v[56:59], v[2:5]
	s_waitcnt lgkmcnt(4)
	v_mfma_f32_16x16x32_bf16 v[6:9], v[64:67], v[60:63], v[6:9]
	s_waitcnt lgkmcnt(3)
	v_mfma_f32_16x16x32_bf16 v[2:5], v[64:67], v[68:71], v[2:5]
	s_waitcnt lgkmcnt(1)
	v_mfma_f32_16x16x32_bf16 v[6:9], v[72:75], v[176:179], v[6:9]
	s_waitcnt lgkmcnt(0)
	v_mfma_f32_16x16x32_bf16 v[2:5], v[72:75], v[180:183], v[2:5]
	v_add_u32_e32 v57, s24, v118
	v_add_u32_e32 v56, s4, v109
	v_add_u32_e32 v58, 0x7ff, v57
	s_cmpk_eq_i32 s4, 0x6c0
	s_cselect_b32 s32, 1, 0
	s_and_b32 s32, s32, s38
	s_add_i32 s4, s4, 64
	s_sub_i32 s24, s24, 64
	v_cndmask_b32_e64 v58, v58, v56, s[76:77]
	s_cmpk_eq_i32 s4, 0x800
	s_waitcnt vmcnt(0)
	s_cselect_b32 s5, 1, 0
	s_cmp_eq_u32 s32, 0
	s_cbranch_scc1 .Les_p3_rest
	v_writelane_b32 v255, 1, 63
	v_readfirstlane_b32 s32, v0
	s_cmp_lg_u32 s32, 0
	s_cbranch_scc1 .Les_p3_rest
	v_readlane_b32 s40, v255, 18
	s_lshl_b32 s40, s40, 10
	s_add_u32 s40, s40, 0x5200
	v_readlane_b32 s41, v255, 5
	s_add_u32 s40, s40, s41
	v_readlane_b32 s41, v255, 6
	s_addc_u32 s41, s41, 0
	s_mov_b64 exec, 1
	global_atomic_add v195, v197, s[40:41]
	s_mov_b64 exec, -1
.Les_p3_rest:
	s_cmp_lg_u32 s5, 0
	s_nop 0
	v_cvt_pk_bf16_f32 v6, v6, v7
	v_cvt_pk_bf16_f32 v7, v8, v9
	v_or_b32_e32 v8, s84, v58
	v_ashrrev_i32_e32 v9, 31, v8
	v_lshl_add_u64 v[8:9], v[8:9], 0, s[2:3]
	v_mad_u64_u32 v[14:15], s[8:9], v8, s11, v[54:55]
	v_mad_i32_i24 v15, v9, s11, v15
	global_store_dwordx2 v[14:15], v[6:7], off
	v_add_u32_e32 v6, 16, v56
	v_add_u32_e32 v7, 0x7ef, v57
	v_cndmask_b32_e64 v6, v7, v6, s[76:77]
	v_cvt_pk_bf16_f32 v2, v2, v3
	v_cvt_pk_bf16_f32 v3, v4, v5
	v_or_b32_e32 v4, s84, v6
	v_ashrrev_i32_e32 v5, 31, v4
	v_lshl_add_u64 v[4:5], v[4:5], 0, s[2:3]
	v_mad_u64_u32 v[6:7], s[8:9], v4, s11, v[54:55]
	v_mad_i32_i24 v7, v5, s11, v7
	global_store_dwordx2 v[6:7], v[2:3], off
	s_cbranch_scc1 .LBB0_448

.LBB0_483:
	v_readlane_b32 s100, v255, 63
	v_writelane_b32 v255, 0, 63
	v_readlane_b32 s0, v255, 18
	v_readlane_b32 s1, v255, 19
	s_lshl_b32 s0, s0, 8
	s_ashr_i32 s1, s0, 31
	s_add_u32 s6, s22, 0x5000
	s_addc_u32 s7, s23, 0
	s_lshl_b64 s[0:1], s[0:1], 2
	s_add_u32 s26, s6, s0
	s_addc_u32 s27, s7, s1
	s_waitcnt vmcnt(0) lgkmcnt(0)
	s_barrier
	s_cmp_lg_u32 s100, 0
	s_cbranch_scc1 .LBB0_542
	s_mov_b64 s[8:9], exec
	v_readlane_b32 s0, v253, 4
	v_readlane_b32 s1, v253, 5
	s_and_b64 s[0:1], s[8:9], s[0:1]
	s_mov_b64 exec, s[0:1]
	s_cbranch_execz .LBB0_486
	s_mov_b64 s[28:29], exec
	v_mbcnt_lo_u32_b32 v1, s28, 0
	v_mbcnt_hi_u32_b32 v1, s29, v1
	v_cmp_eq_u32_e32 vcc, 0, v1
	s_and_b64 s[0:1], exec, vcc
	s_mov_b64 exec, s[0:1]
	s_cbranch_execz .LBB0_486
	s_bcnt1_i32_b64 s0, s[28:29]
	v_mov_b32_e32 v1, s0
	global_atomic_add v195, v1, s[26:27] offset:512

.LBB0_1013:
	v_readlane_b32 s100, v255, 63
	v_writelane_b32 v255, 0, 63
	v_readlane_b32 s4, v255, 18
	s_lshl_b32 s6, s4, 8
	s_ashr_i32 s7, s6, 31
	v_readlane_b32 s5, v255, 19
	s_add_u32 s4, s0, 0x5000
	s_addc_u32 s5, s1, 0
	s_lshl_b64 s[6:7], s[6:7], 2
	s_add_u32 s6, s4, s6
	s_addc_u32 s7, s5, s7
	s_waitcnt vmcnt(0) lgkmcnt(0)
	s_barrier
	s_cmp_lg_u32 s100, 0
	s_cbranch_scc1 .LBB0_1071
	s_mov_b64 s[8:9], exec
	v_readlane_b32 s16, v253, 4
	v_readlane_b32 s17, v253, 5
	s_and_b64 s[16:17], s[8:9], s[16:17]
	s_mov_b64 exec, s[16:17]
	s_cbranch_execz .LBB0_1016
	s_mov_b64 s[22:23], exec
	v_mbcnt_lo_u32_b32 v1, s22, 0
	v_mbcnt_hi_u32_b32 v1, s23, v1
	v_cmp_eq_u32_e32 vcc, 0, v1
	s_and_b64 s[16:17], exec, vcc
	s_mov_b64 exec, s[16:17]
	s_cbranch_execz .LBB0_1016
	s_bcnt1_i32_b64 s2, s[22:23]
	v_mov_b32_e32 v1, s2
	global_atomic_add v195, v1, s[6:7] offset:768

.LBB0_1199:
	v_readlane_b32 s100, v255, 63
	v_writelane_b32 v255, 0, 63
	v_readlane_b32 s6, v255, 18
	s_lshl_b32 s2, s6, 8
	v_readlane_b32 s7, v255, 19
	s_add_i32 s6, s2, 0x100
	s_ashr_i32 s7, s6, 31
	s_add_u32 s46, s28, 0x5000
	s_addc_u32 s47, s29, 0
	s_lshl_b64 s[6:7], s[6:7], 2
	s_add_u32 s6, s46, s6
	s_addc_u32 s7, s47, s7
	s_waitcnt vmcnt(0) lgkmcnt(0)
	s_barrier
	s_cmp_lg_u32 s100, 0
	s_cbranch_scc1 .LBB0_1257
	s_mov_b64 s[8:9], exec
	v_readlane_b32 s16, v253, 4
	v_readlane_b32 s17, v253, 5
	s_and_b64 s[16:17], s[8:9], s[16:17]
	s_mov_b64 exec, s[16:17]
	s_cbranch_execz .LBB0_1202
	s_mov_b64 s[26:27], exec
	v_mbcnt_lo_u32_b32 v1, s26, 0
	v_mbcnt_hi_u32_b32 v1, s27, v1
	v_cmp_eq_u32_e32 vcc, 0, v1
	s_and_b64 s[16:17], exec, vcc
	s_mov_b64 exec, s[16:17]
	s_cbranch_execz .LBB0_1202
	s_bcnt1_i32_b64 s2, s[26:27]
	v_mov_b32_e32 v1, s2
	global_atomic_add v195, v1, s[6:7]
